# early acquire invalidate plus removal of the now-unused per-XCD release atomic on the leader path
# baseline (speedup 1.0000x reference)
; __device__ __forceinline__ unsigned xb_ld(unsigned* p)              { return __hip_atomic_load(p, __ATOMIC_RELAXED, __HIP_MEMORY_SCOPE_AGENT); }
; __device__ __forceinline__ unsigned xb_add(unsigned* p, unsigned v) { return __hip_atomic_fetch_add(p, v, __ATOMIC_RELAXED, __HIP_MEMORY_SCOPE_AGENT); }
; #define XB_SPIN(cond, bar) do { unsigned _sp = 0; while (cond) { __builtin_amdgcn_s_sleep(1); \
;     if ((++_sp & 255u) == 0u) { if (xb_ld(&(bar)[XB_TMO])) break; if (_sp > XB_SPIN_CAP) { atomicAdd(&(bar)[XB_TMO], 1u); break; } } } } while (0)
; __device__ __forceinline__ void xcd_barrier(const XcdBarrier& b) {
;     ...
;             const unsigned tg = og / nx;
;             if (og + 1u == (tg + 1u) * nx) xb_add(&bar[XB_TOPGEN], 1u);
;             else XB_SPIN(xb_ld(&bar[XB_TOPGEN]) == tg, bar);
;             __builtin_amdgcn_fence(__ATOMIC_ACQUIRE, "agent");
;             xb_add(&bar[XB_XGEN(b.x)], 1u);
;             asm volatile("s_waitcnt vmcnt(0)" ::: "memory");
.LBB0_70:
	s_or_b64 exec, exec, s[0:1]
	s_add_i32 s0, s22, 0x900
	s_mov_b32 s1, 0
	s_lshl_b64 s[0:1], s[0:1], 2
	s_add_u32 s0, s38, s0
	s_addc_u32 s1, s39, s1
	v_mov_b32_e32 v1, 1
	v_mov_b64_e32 v[2:3], s[0:1]
	s_waitcnt vmcnt(0) lgkmcnt(0)
	s_waitcnt vmcnt(0)

; __device__ __forceinline__ unsigned xb_ld(unsigned* p)              { return __hip_atomic_load(p, __ATOMIC_RELAXED, __HIP_MEMORY_SCOPE_AGENT); }
; __device__ __forceinline__ unsigned xb_add(unsigned* p, unsigned v) { return __hip_atomic_fetch_add(p, v, __ATOMIC_RELAXED, __HIP_MEMORY_SCOPE_AGENT); }
; #define XB_SPIN(cond, bar) do { unsigned _sp = 0; while (cond) { __builtin_amdgcn_s_sleep(1); \
;     if ((++_sp & 255u) == 0u) { if (xb_ld(&(bar)[XB_TMO])) break; if (_sp > XB_SPIN_CAP) { atomicAdd(&(bar)[XB_TMO], 1u); break; } } } } while (0)
; __device__ __forceinline__ void xcd_barrier(const XcdBarrier& b) {
;     ...
;             const unsigned tg = og / nx;
;             if (og + 1u == (tg + 1u) * nx) xb_add(&bar[XB_TOPGEN], 1u);
;             else XB_SPIN(xb_ld(&bar[XB_TOPGEN]) == tg, bar);
;             __builtin_amdgcn_fence(__ATOMIC_ACQUIRE, "agent");
;             xb_add(&bar[XB_XGEN(b.x)], 1u);
;             asm volatile("s_waitcnt vmcnt(0)" ::: "memory");
.LBB0_205:
	s_or_b64 exec, exec, s[0:1]
	s_add_i32 s0, s22, 0x900
	s_mov_b32 s1, 0
	s_lshl_b64 s[0:1], s[0:1], 2
	s_add_u32 s0, s34, s0
	s_addc_u32 s1, s35, s1
	v_mov_b32_e32 v1, 1
	v_mov_b64_e32 v[2:3], s[0:1]
	s_waitcnt vmcnt(0) lgkmcnt(0)
	s_waitcnt vmcnt(0)

; __device__ __forceinline__ unsigned xb_add(unsigned* p, unsigned v) { return __hip_atomic_fetch_add(p, v, __ATOMIC_RELAXED, __HIP_MEMORY_SCOPE_AGENT); }
; __device__ __forceinline__ void xcd_barrier_host(const XcdBarrier& b, Frame& F, unsigned epoch) {
;     ...
;             __builtin_amdgcn_fence(__ATOMIC_ACQUIRE, "agent");
;             xb_add(&bar[XB_XGEN(b.x)], 1u);
;             asm volatile("s_waitcnt vmcnt(0)" ::: "memory");
.LBB0_275:
	s_or_b64 exec, exec, s[4:5]
	s_add_i32 s4, s24, 0x900
	s_mov_b32 s5, 0
	s_lshl_b64 s[4:5], s[4:5], 2
	s_add_u32 s4, s34, s4
	s_addc_u32 s5, s35, s5
	v_mov_b32_e32 v1, 1
	v_mov_b64_e32 v[2:3], s[4:5]
	s_waitcnt vmcnt(0) lgkmcnt(0)
	s_waitcnt vmcnt(0)

; __device__ __forceinline__ unsigned xb_add(unsigned* p, unsigned v) { return __hip_atomic_fetch_add(p, v, __ATOMIC_RELAXED, __HIP_MEMORY_SCOPE_AGENT); }
; __device__ __forceinline__ void xcd_barrier_host(const XcdBarrier& b, Frame& F, unsigned epoch) {
;     ...
;             __builtin_amdgcn_fence(__ATOMIC_ACQUIRE, "agent");
;             xb_add(&bar[XB_XGEN(b.x)], 1u);
;             asm volatile("s_waitcnt vmcnt(0)" ::: "memory");
.LBB0_281:
	s_or_b64 exec, exec, s[4:5]
	s_add_i32 s94, s24, 0x900
	s_lshl_b64 s[4:5], s[94:95], 2
	s_add_u32 s4, s34, s4
	s_addc_u32 s5, s35, s5
	v_mov_b64_e32 v[2:3], s[4:5]
	s_waitcnt vmcnt(0) lgkmcnt(0)
	s_waitcnt vmcnt(0)

; __device__ __forceinline__ unsigned xb_ld(unsigned* p)              { return __hip_atomic_load(p, __ATOMIC_RELAXED, __HIP_MEMORY_SCOPE_AGENT); }
; __device__ __forceinline__ unsigned xb_add(unsigned* p, unsigned v) { return __hip_atomic_fetch_add(p, v, __ATOMIC_RELAXED, __HIP_MEMORY_SCOPE_AGENT); }
; #define XB_SPIN(cond, bar) do { unsigned _sp = 0; while (cond) { __builtin_amdgcn_s_sleep(1); \
;     if ((++_sp & 255u) == 0u) { if (xb_ld(&(bar)[XB_TMO])) break; if (_sp > XB_SPIN_CAP) { atomicAdd(&(bar)[XB_TMO], 1u); break; } } } } while (0)
; __device__ __forceinline__ void xcd_barrier(const XcdBarrier& b) {
;     ...
;             const unsigned tg = og / nx;
;             if (og + 1u == (tg + 1u) * nx) xb_add(&bar[XB_TOPGEN], 1u);
;             else XB_SPIN(xb_ld(&bar[XB_TOPGEN]) == tg, bar);
;             __builtin_amdgcn_fence(__ATOMIC_ACQUIRE, "agent");
;             xb_add(&bar[XB_XGEN(b.x)], 1u);
;             asm volatile("s_waitcnt vmcnt(0)" ::: "memory");
.LBB0_374:
	s_or_b64 exec, exec, s[0:1]
	s_add_i32 s94, s22, 0x900
	s_lshl_b64 s[0:1], s[94:95], 2
	s_add_u32 s0, s36, s0
	s_addc_u32 s1, s37, s1
	v_mov_b64_e32 v[2:3], s[0:1]
	s_waitcnt vmcnt(0) lgkmcnt(0)
	s_waitcnt vmcnt(0)

; __device__ __forceinline__ unsigned xb_add(unsigned* p, unsigned v) { return __hip_atomic_fetch_add(p, v, __ATOMIC_RELAXED, __HIP_MEMORY_SCOPE_AGENT); }
; __device__ __forceinline__ void xcd_barrier_host(const XcdBarrier& b, Frame& F, unsigned epoch) {
;     ...
;             __builtin_amdgcn_fence(__ATOMIC_ACQUIRE, "agent");
;             xb_add(&bar[XB_XGEN(b.x)], 1u);
;             asm volatile("s_waitcnt vmcnt(0)" ::: "memory");
.LBB0_444:
	s_or_b64 exec, exec, s[4:5]
	s_add_i32 s94, s24, 0x900
	s_lshl_b64 s[4:5], s[94:95], 2
	s_add_u32 s4, s36, s4
	s_addc_u32 s5, s37, s5
	v_mov_b64_e32 v[2:3], s[4:5]
	s_waitcnt vmcnt(0) lgkmcnt(0)
	s_waitcnt vmcnt(0)

; __device__ __forceinline__ unsigned xb_ld(unsigned* p)              { return __hip_atomic_load(p, __ATOMIC_RELAXED, __HIP_MEMORY_SCOPE_AGENT); }
; __device__ __forceinline__ unsigned xb_add(unsigned* p, unsigned v) { return __hip_atomic_fetch_add(p, v, __ATOMIC_RELAXED, __HIP_MEMORY_SCOPE_AGENT); }
; #define XB_SPIN(cond, bar) do { unsigned _sp = 0; while (cond) { __builtin_amdgcn_s_sleep(1); \
;     if ((++_sp & 255u) == 0u) { if (xb_ld(&(bar)[XB_TMO])) break; if (_sp > XB_SPIN_CAP) { atomicAdd(&(bar)[XB_TMO], 1u); break; } } } } while (0)
; __device__ __forceinline__ void xcd_barrier(const XcdBarrier& b) {
;     ...
;             const unsigned tg = og / nx;
;             if (og + 1u == (tg + 1u) * nx) xb_add(&bar[XB_TOPGEN], 1u);
;             else XB_SPIN(xb_ld(&bar[XB_TOPGEN]) == tg, bar);
;             __builtin_amdgcn_fence(__ATOMIC_ACQUIRE, "agent");
;             xb_add(&bar[XB_XGEN(b.x)], 1u);
;             asm volatile("s_waitcnt vmcnt(0)" ::: "memory");
.LBB0_2041:
	s_or_b64 exec, exec, s[0:1]
	s_add_i32 s94, s22, 0x900
	s_lshl_b64 s[0:1], s[94:95], 2
	s_add_u32 s0, s34, s0
	s_addc_u32 s1, s35, s1
	v_mov_b64_e32 v[2:3], s[0:1]
	s_waitcnt vmcnt(0) lgkmcnt(0)
	s_waitcnt vmcnt(0)
